# speedup vs baseline: 1.0132x; 1.0132x over previous
.Lg1_w03:
	v_and_b32_e32 v98, 15, v0
	v_bfe_u32 v97, v0, 4, 2
	v_lshrrev_b32_e32 v96, 7, v0
	v_bfe_u32 v1, v0, 6, 1
	v_bfe_u32 v95, v0, 1, 3
	v_xor_b32_e32 v95, v97, v95
	v_lshlrev_b32_e32 v95, 4, v95
	v_lshl_or_b32 v99, v98, 7, v95
	v_lshl_or_b32 v89, v96, 13, v99
	v_mul_u32_u24_e32 v95, 0x2800, v1
	v_add_u32_e32 v95, 0x8000, v95
	v_add_u32_e32 v90, v95, v99
	s_waitcnt lgkmcnt(0)
	s_mov_b32 s22, s12
	s_mov_b32 s23, s13
	s_mov_b32 s24, s14
	s_mov_b32 s25, s15
	s_mov_b32 s26, s20
	s_add_i32 s30, s26, s29
	s_mov_b32 m0, s26
	s_add_i32 s26, s26, 0x2000
	global_load_lds_dwordx4 v82, s[22:23]
	s_mov_b32 m0, s26
	s_add_i32 s26, s26, 0x2000
	global_load_lds_dwordx4 v83, s[22:23]
	s_mov_b32 m0, s26
	s_add_i32 s26, s26, 0x2000
	global_load_lds_dwordx4 v84, s[22:23]
	s_mov_b32 m0, s26
	s_add_i32 s26, s26, 0x2000
	global_load_lds_dwordx4 v85, s[22:23]
	s_mov_b32 m0, s26
	s_add_i32 s26, s26, 0x2000
	global_load_lds_dwordx4 v86, s[24:25]
	s_mov_b32 m0, s26
	s_add_i32 s26, s26, 0x2000
	global_load_lds_dwordx4 v87, s[24:25]
	s_mov_b32 m0, s30
	s_add_i32 s26, s26, 0x1000
	global_load_lds_dwordx4 v88, s[24:25]
	s_add_u32 s22, s22, 0x80
	s_addc_u32 s23, s23, 0
	s_add_u32 s24, s24, 0x80
	s_addc_u32 s25, s25, 0
	s_add_i32 s30, s26, s29
	s_mov_b32 m0, s26
	s_add_i32 s26, s26, 0x2000
	global_load_lds_dwordx4 v82, s[22:23]
	s_mov_b32 m0, s26
	s_add_i32 s26, s26, 0x2000
	global_load_lds_dwordx4 v83, s[22:23]
	s_mov_b32 m0, s26
	s_add_i32 s26, s26, 0x2000
	global_load_lds_dwordx4 v84, s[22:23]
	s_mov_b32 m0, s26
	s_add_i32 s26, s26, 0x2000
	global_load_lds_dwordx4 v85, s[22:23]
	s_mov_b32 m0, s26
	s_add_i32 s26, s26, 0x2000
	global_load_lds_dwordx4 v86, s[24:25]
	s_mov_b32 m0, s26
	s_add_i32 s26, s26, 0x2000
	global_load_lds_dwordx4 v87, s[24:25]
	s_mov_b32 m0, s30
	s_add_i32 s26, s26, 0x1000
	global_load_lds_dwordx4 v88, s[24:25]
	s_add_u32 s22, s22, 0x80
	s_addc_u32 s23, s23, 0
	s_add_u32 s24, s24, 0x80
	s_addc_u32 s25, s25, 0
	s_add_i32 s30, s26, s29
	s_mov_b32 m0, s26
	s_add_i32 s26, s26, 0x2000
	global_load_lds_dwordx4 v82, s[22:23]
	s_mov_b32 m0, s26
	s_add_i32 s26, s26, 0x2000
	global_load_lds_dwordx4 v83, s[22:23]
	s_mov_b32 m0, s26
	s_add_i32 s26, s26, 0x2000
	global_load_lds_dwordx4 v84, s[22:23]
	s_mov_b32 m0, s26
	s_add_i32 s26, s26, 0x2000
	global_load_lds_dwordx4 v85, s[22:23]
	s_mov_b32 m0, s26
	s_add_i32 s26, s26, 0x2000
	global_load_lds_dwordx4 v86, s[24:25]
	s_mov_b32 m0, s26
	s_add_i32 s26, s26, 0x2000
	global_load_lds_dwordx4 v87, s[24:25]
	s_mov_b32 m0, s30
	s_add_i32 s26, s26, 0x1000
	global_load_lds_dwordx4 v88, s[24:25]
	v_mov_b32_e32 v2, 0
	v_mov_b32_e32 v3, 0
	v_mov_b32_e32 v4, 0
	v_mov_b32_e32 v5, 0
	v_mov_b32_e32 v6, 0
	v_mov_b32_e32 v7, 0
	v_mov_b32_e32 v8, 0
	v_mov_b32_e32 v9, 0
	v_mov_b32_e32 v10, 0
	v_mov_b32_e32 v11, 0
	v_mov_b32_e32 v12, 0
	v_mov_b32_e32 v13, 0
	v_mov_b32_e32 v14, 0
	v_mov_b32_e32 v15, 0
	v_mov_b32_e32 v16, 0
	v_mov_b32_e32 v17, 0
	v_mov_b32_e32 v18, 0
	v_mov_b32_e32 v19, 0
	v_mov_b32_e32 v20, 0
	v_mov_b32_e32 v21, 0
	v_mov_b32_e32 v22, 0
	v_mov_b32_e32 v23, 0
	v_mov_b32_e32 v24, 0
	v_mov_b32_e32 v25, 0
	v_mov_b32_e32 v26, 0
	v_mov_b32_e32 v27, 0
	v_mov_b32_e32 v28, 0
	v_mov_b32_e32 v29, 0
	v_mov_b32_e32 v30, 0
	v_mov_b32_e32 v31, 0
	v_mov_b32_e32 v32, 0
	v_mov_b32_e32 v33, 0
	v_mov_b32_e32 v34, 0
	v_mov_b32_e32 v35, 0
	v_mov_b32_e32 v36, 0
	v_mov_b32_e32 v37, 0
	v_mov_b32_e32 v38, 0
	v_mov_b32_e32 v39, 0
	v_mov_b32_e32 v40, 0
	v_mov_b32_e32 v41, 0
	v_mov_b32_e32 v42, 0
	v_mov_b32_e32 v43, 0
	v_mov_b32_e32 v44, 0
	v_mov_b32_e32 v45, 0
	v_mov_b32_e32 v46, 0
	v_mov_b32_e32 v47, 0
	v_mov_b32_e32 v48, 0
	v_mov_b32_e32 v49, 0
	v_mov_b32_e32 v50, 0
	v_mov_b32_e32 v51, 0
	v_mov_b32_e32 v52, 0
	v_mov_b32_e32 v53, 0
	v_mov_b32_e32 v54, 0
	v_mov_b32_e32 v55, 0
	v_mov_b32_e32 v56, 0
	v_mov_b32_e32 v57, 0
	v_mov_b32_e32 v58, 0
	v_mov_b32_e32 v59, 0
	v_mov_b32_e32 v60, 0
	v_mov_b32_e32 v61, 0
	v_mov_b32_e32 v62, 0
	v_mov_b32_e32 v63, 0
	v_mov_b32_e32 v64, 0
	v_mov_b32_e32 v65, 0
	v_mov_b32_e32 v66, 0
	v_mov_b32_e32 v67, 0
	v_mov_b32_e32 v68, 0
	v_mov_b32_e32 v69, 0
	v_mov_b32_e32 v70, 0
	v_mov_b32_e32 v71, 0
	v_mov_b32_e32 v72, 0
	v_mov_b32_e32 v73, 0
	v_mov_b32_e32 v74, 0
	v_mov_b32_e32 v75, 0
	v_mov_b32_e32 v76, 0
	v_mov_b32_e32 v77, 0
	v_mov_b32_e32 v78, 0
	v_mov_b32_e32 v79, 0
	v_mov_b32_e32 v80, 0
	v_mov_b32_e32 v81, 0
	s_mov_b32 s16, 0
	s_mov_b32 s17, 0
	v_mov_b32_e32 v91, v89
	v_mov_b32_e32 v93, v90
	v_xor_b32_e32 v92, 64, v89
	v_xor_b32_e32 v94, 64, v90
	s_waitcnt vmcnt(14)
	s_barrier
	ds_read_b128 v[116:119], v93
	ds_read_b128 v[100:103], v91
	ds_read_b128 v[120:123], v93 offset:2048
	ds_read_b128 v[104:107], v91 offset:2048
	ds_read_b128 v[124:127], v93 offset:4096
	ds_read_b128 v[108:111], v91 offset:4096
	ds_read_b128 v[128:131], v93 offset:6144
	ds_read_b128 v[112:115], v91 offset:6144
	ds_read_b128 v[132:135], v93 offset:8192
	s_add_i32 s27, s17, 0xd000
	s_cmp_lg_u32 s27, 0x27000
	s_cselect_b32 s27, s27, 0
	s_waitcnt lgkmcnt(0)
	v_mfma_f32_16x16x32_f16 v[34:37], v[116:119], v[100:103], v[34:37]
	ds_read_b128 v[152:155], v94
	v_mfma_f32_16x16x32_f16 v[78:81], v[120:123], v[100:103], v[78:81]
	ds_read_b128 v[136:139], v92
	v_mfma_f32_16x16x32_f16 v[74:77], v[124:127], v[100:103], v[74:77]
	ds_read_b128 v[156:159], v94 offset:2048
	v_mfma_f32_16x16x32_f16 v[70:73], v[128:131], v[100:103], v[70:73]
	ds_read_b128 v[140:143], v92 offset:2048
	v_mfma_f32_16x16x32_f16 v[62:65], v[132:135], v[100:103], v[62:65]
	ds_read_b128 v[160:163], v94 offset:4096
	v_mfma_f32_16x16x32_f16 v[58:61], v[116:119], v[104:107], v[58:61]
	ds_read_b128 v[144:147], v92 offset:4096
	v_mfma_f32_16x16x32_f16 v[54:57], v[120:123], v[104:107], v[54:57]
	ds_read_b128 v[164:167], v94 offset:6144
	v_mfma_f32_16x16x32_f16 v[50:53], v[124:127], v[104:107], v[50:53]
	ds_read_b128 v[148:151], v92 offset:6144
	v_mfma_f32_16x16x32_f16 v[46:49], v[128:131], v[104:107], v[46:49]
	ds_read_b128 v[168:171], v94 offset:8192
	v_mfma_f32_16x16x32_f16 v[42:45], v[132:135], v[104:107], v[42:45]
	v_mfma_f32_16x16x32_f16 v[38:41], v[116:119], v[108:111], v[38:41]
	v_add_u32_e32 v91, s27, v89
	v_mfma_f32_16x16x32_f16 v[30:33], v[120:123], v[108:111], v[30:33]
	v_add_u32_e32 v93, s27, v90
	v_mfma_f32_16x16x32_f16 v[26:29], v[124:127], v[108:111], v[26:29]
	v_xor_b32_e32 v92, 64, v91
	v_mfma_f32_16x16x32_f16 v[22:25], v[128:131], v[108:111], v[22:25]
	v_xor_b32_e32 v94, 64, v93
	v_mfma_f32_16x16x32_f16 v[18:21], v[132:135], v[108:111], v[18:21]
	v_mfma_f32_16x16x32_f16 v[14:17], v[116:119], v[112:115], v[14:17]
	v_mfma_f32_16x16x32_f16 v[10:13], v[120:123], v[112:115], v[10:13]
	v_mfma_f32_16x16x32_f16 v[2:5], v[124:127], v[112:115], v[2:5]
	v_mfma_f32_16x16x32_f16 v[6:9], v[128:131], v[112:115], v[6:9]
	v_mfma_f32_16x16x32_f16 v[66:69], v[132:135], v[112:115], v[66:69]
	s_waitcnt vmcnt(7)
	s_waitcnt lgkmcnt(0)
	s_barrier
	s_add_i32 s18, s16, 3
	s_lshl_b32 s18, s18, 7
	s_add_u32 s22, s12, s18
	s_addc_u32 s23, s13, 0
	s_add_u32 s24, s14, s18
	s_addc_u32 s25, s15, 0
	s_add_i32 s26, s17, s20
	s_add_i32 s30, s26, s29
	v_mfma_f32_16x16x32_f16 v[34:37], v[152:155], v[136:139], v[34:37]
	ds_read_b128 v[116:119], v93
	v_mfma_f32_16x16x32_f16 v[78:81], v[156:159], v[136:139], v[78:81]
	ds_read_b128 v[100:103], v91
	v_mfma_f32_16x16x32_f16 v[74:77], v[160:163], v[136:139], v[74:77]
	ds_read_b128 v[120:123], v93 offset:2048
	v_mfma_f32_16x16x32_f16 v[70:73], v[164:167], v[136:139], v[70:73]
	ds_read_b128 v[104:107], v91 offset:2048
	v_mfma_f32_16x16x32_f16 v[62:65], v[168:171], v[136:139], v[62:65]
	ds_read_b128 v[124:127], v93 offset:4096
	v_mfma_f32_16x16x32_f16 v[58:61], v[152:155], v[140:143], v[58:61]
	ds_read_b128 v[108:111], v91 offset:4096
	v_mfma_f32_16x16x32_f16 v[54:57], v[156:159], v[140:143], v[54:57]
	ds_read_b128 v[128:131], v93 offset:6144
	v_mfma_f32_16x16x32_f16 v[50:53], v[160:163], v[140:143], v[50:53]
	ds_read_b128 v[112:115], v91 offset:6144
	v_mfma_f32_16x16x32_f16 v[46:49], v[164:167], v[140:143], v[46:49]
	ds_read_b128 v[132:135], v93 offset:8192
	v_mfma_f32_16x16x32_f16 v[42:45], v[168:171], v[140:143], v[42:45]
	v_mfma_f32_16x16x32_f16 v[38:41], v[152:155], v[144:147], v[38:41]
	s_mov_b32 m0, s26
	s_add_i32 s26, s26, 0x2000
	global_load_lds_dwordx4 v82, s[22:23]
	v_mfma_f32_16x16x32_f16 v[30:33], v[156:159], v[144:147], v[30:33]
	v_mfma_f32_16x16x32_f16 v[26:29], v[160:163], v[144:147], v[26:29]
	v_mfma_f32_16x16x32_f16 v[22:25], v[164:167], v[144:147], v[22:25]
	s_mov_b32 m0, s26
	s_add_i32 s26, s26, 0x2000
	global_load_lds_dwordx4 v83, s[22:23]
	v_mfma_f32_16x16x32_f16 v[18:21], v[168:171], v[144:147], v[18:21]
	v_mfma_f32_16x16x32_f16 v[14:17], v[152:155], v[148:151], v[14:17]
	v_mfma_f32_16x16x32_f16 v[10:13], v[156:159], v[148:151], v[10:13]
	s_mov_b32 m0, s26
	s_add_i32 s26, s26, 0x2000
	global_load_lds_dwordx4 v84, s[22:23]
	v_mfma_f32_16x16x32_f16 v[2:5], v[160:163], v[148:151], v[2:5]
	v_mfma_f32_16x16x32_f16 v[6:9], v[164:167], v[148:151], v[6:9]
	v_mfma_f32_16x16x32_f16 v[66:69], v[168:171], v[148:151], v[66:69]
	s_mov_b32 m0, s26
	s_add_i32 s26, s26, 0x2000
	global_load_lds_dwordx4 v85, s[22:23]
	s_mov_b32 s17, s27
	s_add_i32 s16, s16, 1
.Lg1_loop:
	s_add_i32 s27, s17, 0xd000
	s_cmp_lg_u32 s27, 0x27000
	s_cselect_b32 s27, s27, 0
	s_waitcnt lgkmcnt(0)
	v_mfma_f32_16x16x32_f16 v[34:37], v[116:119], v[100:103], v[34:37]
	ds_read_b128 v[152:155], v94
	v_mfma_f32_16x16x32_f16 v[78:81], v[120:123], v[100:103], v[78:81]
	ds_read_b128 v[136:139], v92
	v_mfma_f32_16x16x32_f16 v[74:77], v[124:127], v[100:103], v[74:77]
	ds_read_b128 v[156:159], v94 offset:2048
	v_mfma_f32_16x16x32_f16 v[70:73], v[128:131], v[100:103], v[70:73]
	ds_read_b128 v[140:143], v92 offset:2048
	v_mfma_f32_16x16x32_f16 v[62:65], v[132:135], v[100:103], v[62:65]
	ds_read_b128 v[160:163], v94 offset:4096
	v_mfma_f32_16x16x32_f16 v[58:61], v[116:119], v[104:107], v[58:61]
	ds_read_b128 v[144:147], v92 offset:4096
	v_mfma_f32_16x16x32_f16 v[54:57], v[120:123], v[104:107], v[54:57]
	ds_read_b128 v[164:167], v94 offset:6144
	v_mfma_f32_16x16x32_f16 v[50:53], v[124:127], v[104:107], v[50:53]
	ds_read_b128 v[148:151], v92 offset:6144
	v_mfma_f32_16x16x32_f16 v[46:49], v[128:131], v[104:107], v[46:49]
	ds_read_b128 v[168:171], v94 offset:8192
	v_mfma_f32_16x16x32_f16 v[42:45], v[132:135], v[104:107], v[42:45]
	v_mfma_f32_16x16x32_f16 v[38:41], v[116:119], v[108:111], v[38:41]
	v_add_u32_e32 v91, s27, v89
	v_mfma_f32_16x16x32_f16 v[30:33], v[120:123], v[108:111], v[30:33]
	v_add_u32_e32 v93, s27, v90
	v_mfma_f32_16x16x32_f16 v[26:29], v[124:127], v[108:111], v[26:29]
	v_xor_b32_e32 v92, 64, v91
	v_mfma_f32_16x16x32_f16 v[22:25], v[128:131], v[108:111], v[22:25]
	v_xor_b32_e32 v94, 64, v93
	v_mfma_f32_16x16x32_f16 v[18:21], v[132:135], v[108:111], v[18:21]
	s_mov_b32 m0, s26
	s_add_i32 s26, s26, 0x2000
	global_load_lds_dwordx4 v86, s[24:25]
	v_mfma_f32_16x16x32_f16 v[14:17], v[116:119], v[112:115], v[14:17]
	v_mfma_f32_16x16x32_f16 v[10:13], v[120:123], v[112:115], v[10:13]
	s_mov_b32 m0, s26
	s_nop 0
	global_load_lds_dwordx4 v87, s[24:25]
	v_mfma_f32_16x16x32_f16 v[2:5], v[124:127], v[112:115], v[2:5]
	v_mfma_f32_16x16x32_f16 v[6:9], v[128:131], v[112:115], v[6:9]
	s_mov_b32 m0, s30
	s_nop 0
	global_load_lds_dwordx4 v88, s[24:25]
	v_mfma_f32_16x16x32_f16 v[66:69], v[132:135], v[112:115], v[66:69]
	s_waitcnt vmcnt(7)
	s_waitcnt lgkmcnt(0)
	s_barrier
	s_add_i32 s18, s16, 3
	s_lshl_b32 s18, s18, 7
	s_add_u32 s22, s12, s18
	s_addc_u32 s23, s13, 0
	s_add_u32 s24, s14, s18
	s_addc_u32 s25, s15, 0
	s_add_i32 s26, s17, s20
	s_add_i32 s30, s26, s29
	v_mfma_f32_16x16x32_f16 v[34:37], v[152:155], v[136:139], v[34:37]
	ds_read_b128 v[116:119], v93
	v_mfma_f32_16x16x32_f16 v[78:81], v[156:159], v[136:139], v[78:81]
	ds_read_b128 v[100:103], v91
	v_mfma_f32_16x16x32_f16 v[74:77], v[160:163], v[136:139], v[74:77]
	ds_read_b128 v[120:123], v93 offset:2048
	v_mfma_f32_16x16x32_f16 v[70:73], v[164:167], v[136:139], v[70:73]
	ds_read_b128 v[104:107], v91 offset:2048
	v_mfma_f32_16x16x32_f16 v[62:65], v[168:171], v[136:139], v[62:65]
	ds_read_b128 v[124:127], v93 offset:4096
	v_mfma_f32_16x16x32_f16 v[58:61], v[152:155], v[140:143], v[58:61]
	ds_read_b128 v[108:111], v91 offset:4096
	v_mfma_f32_16x16x32_f16 v[54:57], v[156:159], v[140:143], v[54:57]
	ds_read_b128 v[128:131], v93 offset:6144
	v_mfma_f32_16x16x32_f16 v[50:53], v[160:163], v[140:143], v[50:53]
	ds_read_b128 v[112:115], v91 offset:6144
	v_mfma_f32_16x16x32_f16 v[46:49], v[164:167], v[140:143], v[46:49]
	ds_read_b128 v[132:135], v93 offset:8192
	v_mfma_f32_16x16x32_f16 v[42:45], v[168:171], v[140:143], v[42:45]
	v_mfma_f32_16x16x32_f16 v[38:41], v[152:155], v[144:147], v[38:41]
	s_mov_b32 m0, s26
	s_add_i32 s26, s26, 0x2000
	global_load_lds_dwordx4 v82, s[22:23]
	v_mfma_f32_16x16x32_f16 v[30:33], v[156:159], v[144:147], v[30:33]
	v_mfma_f32_16x16x32_f16 v[26:29], v[160:163], v[144:147], v[26:29]
	v_mfma_f32_16x16x32_f16 v[22:25], v[164:167], v[144:147], v[22:25]
	s_mov_b32 m0, s26
	s_add_i32 s26, s26, 0x2000
	global_load_lds_dwordx4 v83, s[22:23]
	v_mfma_f32_16x16x32_f16 v[18:21], v[168:171], v[144:147], v[18:21]
	v_mfma_f32_16x16x32_f16 v[14:17], v[152:155], v[148:151], v[14:17]
	v_mfma_f32_16x16x32_f16 v[10:13], v[156:159], v[148:151], v[10:13]
	s_mov_b32 m0, s26
	s_add_i32 s26, s26, 0x2000
	global_load_lds_dwordx4 v84, s[22:23]
	v_mfma_f32_16x16x32_f16 v[2:5], v[160:163], v[148:151], v[2:5]
	v_mfma_f32_16x16x32_f16 v[6:9], v[164:167], v[148:151], v[6:9]
	v_mfma_f32_16x16x32_f16 v[66:69], v[168:171], v[148:151], v[66:69]
	s_mov_b32 m0, s26
	s_add_i32 s26, s26, 0x2000
	global_load_lds_dwordx4 v85, s[22:23]
	s_mov_b32 s17, s27
	s_add_i32 s16, s16, 1
	s_cmp_lt_u32 s16, 13
	s_cbranch_scc1 .Lg1_loop
	s_add_i32 s27, s17, 0xd000
	s_cmp_lg_u32 s27, 0x27000
	s_cselect_b32 s27, s27, 0
	s_waitcnt lgkmcnt(0)
	v_mfma_f32_16x16x32_f16 v[34:37], v[116:119], v[100:103], v[34:37]
	ds_read_b128 v[152:155], v94
	v_mfma_f32_16x16x32_f16 v[78:81], v[120:123], v[100:103], v[78:81]
	ds_read_b128 v[136:139], v92
	v_mfma_f32_16x16x32_f16 v[74:77], v[124:127], v[100:103], v[74:77]
	ds_read_b128 v[156:159], v94 offset:2048
	v_mfma_f32_16x16x32_f16 v[70:73], v[128:131], v[100:103], v[70:73]
	ds_read_b128 v[140:143], v92 offset:2048
	v_mfma_f32_16x16x32_f16 v[62:65], v[132:135], v[100:103], v[62:65]
	ds_read_b128 v[160:163], v94 offset:4096
	v_mfma_f32_16x16x32_f16 v[58:61], v[116:119], v[104:107], v[58:61]
	ds_read_b128 v[144:147], v92 offset:4096
	v_mfma_f32_16x16x32_f16 v[54:57], v[120:123], v[104:107], v[54:57]
	ds_read_b128 v[164:167], v94 offset:6144
	v_mfma_f32_16x16x32_f16 v[50:53], v[124:127], v[104:107], v[50:53]
	ds_read_b128 v[148:151], v92 offset:6144
	v_mfma_f32_16x16x32_f16 v[46:49], v[128:131], v[104:107], v[46:49]
	ds_read_b128 v[168:171], v94 offset:8192
	v_mfma_f32_16x16x32_f16 v[42:45], v[132:135], v[104:107], v[42:45]
	v_mfma_f32_16x16x32_f16 v[38:41], v[116:119], v[108:111], v[38:41]
	v_add_u32_e32 v91, s27, v89
	v_mfma_f32_16x16x32_f16 v[30:33], v[120:123], v[108:111], v[30:33]
	v_add_u32_e32 v93, s27, v90
	v_mfma_f32_16x16x32_f16 v[26:29], v[124:127], v[108:111], v[26:29]
	v_xor_b32_e32 v92, 64, v91
	v_mfma_f32_16x16x32_f16 v[22:25], v[128:131], v[108:111], v[22:25]
	v_xor_b32_e32 v94, 64, v93
	v_mfma_f32_16x16x32_f16 v[18:21], v[132:135], v[108:111], v[18:21]
	s_mov_b32 m0, s26
	s_add_i32 s26, s26, 0x2000
	global_load_lds_dwordx4 v86, s[24:25]
	v_mfma_f32_16x16x32_f16 v[14:17], v[116:119], v[112:115], v[14:17]
	v_mfma_f32_16x16x32_f16 v[10:13], v[120:123], v[112:115], v[10:13]
	s_mov_b32 m0, s26
	s_nop 0
	global_load_lds_dwordx4 v87, s[24:25]
	v_mfma_f32_16x16x32_f16 v[2:5], v[124:127], v[112:115], v[2:5]
	v_mfma_f32_16x16x32_f16 v[6:9], v[128:131], v[112:115], v[6:9]
	s_mov_b32 m0, s30
	s_nop 0
	global_load_lds_dwordx4 v88, s[24:25]
	v_mfma_f32_16x16x32_f16 v[66:69], v[132:135], v[112:115], v[66:69]
	s_waitcnt vmcnt(7)
	s_waitcnt lgkmcnt(0)
	s_barrier
	v_mfma_f32_16x16x32_f16 v[34:37], v[152:155], v[136:139], v[34:37]
	ds_read_b128 v[116:119], v93
	v_mfma_f32_16x16x32_f16 v[78:81], v[156:159], v[136:139], v[78:81]
	ds_read_b128 v[100:103], v91
	v_mfma_f32_16x16x32_f16 v[74:77], v[160:163], v[136:139], v[74:77]
	ds_read_b128 v[120:123], v93 offset:2048
	v_mfma_f32_16x16x32_f16 v[70:73], v[164:167], v[136:139], v[70:73]
	ds_read_b128 v[104:107], v91 offset:2048
	v_mfma_f32_16x16x32_f16 v[62:65], v[168:171], v[136:139], v[62:65]
	ds_read_b128 v[124:127], v93 offset:4096
	v_mfma_f32_16x16x32_f16 v[58:61], v[152:155], v[140:143], v[58:61]
	ds_read_b128 v[108:111], v91 offset:4096
	v_mfma_f32_16x16x32_f16 v[54:57], v[156:159], v[140:143], v[54:57]
	ds_read_b128 v[128:131], v93 offset:6144
	v_mfma_f32_16x16x32_f16 v[50:53], v[160:163], v[140:143], v[50:53]
	ds_read_b128 v[112:115], v91 offset:6144
	v_mfma_f32_16x16x32_f16 v[46:49], v[164:167], v[140:143], v[46:49]
	ds_read_b128 v[132:135], v93 offset:8192
	v_mfma_f32_16x16x32_f16 v[42:45], v[168:171], v[140:143], v[42:45]
	v_mfma_f32_16x16x32_f16 v[38:41], v[152:155], v[144:147], v[38:41]
	v_mfma_f32_16x16x32_f16 v[30:33], v[156:159], v[144:147], v[30:33]
	v_mfma_f32_16x16x32_f16 v[26:29], v[160:163], v[144:147], v[26:29]
	v_mfma_f32_16x16x32_f16 v[22:25], v[164:167], v[144:147], v[22:25]
	v_mfma_f32_16x16x32_f16 v[18:21], v[168:171], v[144:147], v[18:21]
	v_mfma_f32_16x16x32_f16 v[14:17], v[152:155], v[148:151], v[14:17]
	v_mfma_f32_16x16x32_f16 v[10:13], v[156:159], v[148:151], v[10:13]
	v_mfma_f32_16x16x32_f16 v[2:5], v[160:163], v[148:151], v[2:5]
	v_mfma_f32_16x16x32_f16 v[6:9], v[164:167], v[148:151], v[6:9]
	v_mfma_f32_16x16x32_f16 v[66:69], v[168:171], v[148:151], v[66:69]
	s_mov_b32 s17, s27
	s_add_i32 s16, s16, 1
	s_add_i32 s27, s17, 0xd000
	s_cmp_lg_u32 s27, 0x27000
	s_cselect_b32 s27, s27, 0
	s_waitcnt lgkmcnt(0)
	v_mfma_f32_16x16x32_f16 v[34:37], v[116:119], v[100:103], v[34:37]
	ds_read_b128 v[152:155], v94
	v_mfma_f32_16x16x32_f16 v[78:81], v[120:123], v[100:103], v[78:81]
	ds_read_b128 v[136:139], v92
	v_mfma_f32_16x16x32_f16 v[74:77], v[124:127], v[100:103], v[74:77]
	ds_read_b128 v[156:159], v94 offset:2048
	v_mfma_f32_16x16x32_f16 v[70:73], v[128:131], v[100:103], v[70:73]
	ds_read_b128 v[140:143], v92 offset:2048
	v_mfma_f32_16x16x32_f16 v[62:65], v[132:135], v[100:103], v[62:65]
	ds_read_b128 v[160:163], v94 offset:4096
	v_mfma_f32_16x16x32_f16 v[58:61], v[116:119], v[104:107], v[58:61]
	ds_read_b128 v[144:147], v92 offset:4096
	v_mfma_f32_16x16x32_f16 v[54:57], v[120:123], v[104:107], v[54:57]
	ds_read_b128 v[164:167], v94 offset:6144
	v_mfma_f32_16x16x32_f16 v[50:53], v[124:127], v[104:107], v[50:53]
	ds_read_b128 v[148:151], v92 offset:6144
	v_mfma_f32_16x16x32_f16 v[46:49], v[128:131], v[104:107], v[46:49]
	ds_read_b128 v[168:171], v94 offset:8192
	v_mfma_f32_16x16x32_f16 v[42:45], v[132:135], v[104:107], v[42:45]
	v_mfma_f32_16x16x32_f16 v[38:41], v[116:119], v[108:111], v[38:41]
	v_add_u32_e32 v91, s27, v89
	v_mfma_f32_16x16x32_f16 v[30:33], v[120:123], v[108:111], v[30:33]
	v_add_u32_e32 v93, s27, v90
	v_mfma_f32_16x16x32_f16 v[26:29], v[124:127], v[108:111], v[26:29]
	v_xor_b32_e32 v92, 64, v91
	v_mfma_f32_16x16x32_f16 v[22:25], v[128:131], v[108:111], v[22:25]
	v_xor_b32_e32 v94, 64, v93
	v_mfma_f32_16x16x32_f16 v[18:21], v[132:135], v[108:111], v[18:21]
	v_mfma_f32_16x16x32_f16 v[14:17], v[116:119], v[112:115], v[14:17]
	v_mfma_f32_16x16x32_f16 v[10:13], v[120:123], v[112:115], v[10:13]
	v_mfma_f32_16x16x32_f16 v[2:5], v[124:127], v[112:115], v[2:5]
	v_mfma_f32_16x16x32_f16 v[6:9], v[128:131], v[112:115], v[6:9]
	v_mfma_f32_16x16x32_f16 v[66:69], v[132:135], v[112:115], v[66:69]
	s_waitcnt vmcnt(0)
	s_waitcnt lgkmcnt(0)
	s_barrier
	v_mfma_f32_16x16x32_f16 v[34:37], v[152:155], v[136:139], v[34:37]
	ds_read_b128 v[116:119], v93
	v_mfma_f32_16x16x32_f16 v[78:81], v[156:159], v[136:139], v[78:81]
	ds_read_b128 v[100:103], v91
	v_mfma_f32_16x16x32_f16 v[74:77], v[160:163], v[136:139], v[74:77]
	ds_read_b128 v[120:123], v93 offset:2048
	v_mfma_f32_16x16x32_f16 v[70:73], v[164:167], v[136:139], v[70:73]
	ds_read_b128 v[104:107], v91 offset:2048
	v_mfma_f32_16x16x32_f16 v[62:65], v[168:171], v[136:139], v[62:65]
	ds_read_b128 v[124:127], v93 offset:4096
	v_mfma_f32_16x16x32_f16 v[58:61], v[152:155], v[140:143], v[58:61]
	ds_read_b128 v[108:111], v91 offset:4096
	v_mfma_f32_16x16x32_f16 v[54:57], v[156:159], v[140:143], v[54:57]
	ds_read_b128 v[128:131], v93 offset:6144
	v_mfma_f32_16x16x32_f16 v[50:53], v[160:163], v[140:143], v[50:53]
	ds_read_b128 v[112:115], v91 offset:6144
	v_mfma_f32_16x16x32_f16 v[46:49], v[164:167], v[140:143], v[46:49]
	ds_read_b128 v[132:135], v93 offset:8192
	v_mfma_f32_16x16x32_f16 v[42:45], v[168:171], v[140:143], v[42:45]
	v_mfma_f32_16x16x32_f16 v[38:41], v[152:155], v[144:147], v[38:41]
	v_mfma_f32_16x16x32_f16 v[30:33], v[156:159], v[144:147], v[30:33]
	v_mfma_f32_16x16x32_f16 v[26:29], v[160:163], v[144:147], v[26:29]
	v_mfma_f32_16x16x32_f16 v[22:25], v[164:167], v[144:147], v[22:25]
	v_mfma_f32_16x16x32_f16 v[18:21], v[168:171], v[144:147], v[18:21]
	v_mfma_f32_16x16x32_f16 v[14:17], v[152:155], v[148:151], v[14:17]
	v_mfma_f32_16x16x32_f16 v[10:13], v[156:159], v[148:151], v[10:13]
	v_mfma_f32_16x16x32_f16 v[2:5], v[160:163], v[148:151], v[2:5]
	v_mfma_f32_16x16x32_f16 v[6:9], v[164:167], v[148:151], v[6:9]
	v_mfma_f32_16x16x32_f16 v[66:69], v[168:171], v[148:151], v[66:69]
	s_mov_b32 s17, s27
	s_add_i32 s16, s16, 1
	s_add_i32 s27, s17, 0xd000
	s_cmp_lg_u32 s27, 0x27000
	s_cselect_b32 s27, s27, 0
	s_waitcnt lgkmcnt(0)
	v_mfma_f32_16x16x32_f16 v[34:37], v[116:119], v[100:103], v[34:37]
	ds_read_b128 v[152:155], v94
	v_mfma_f32_16x16x32_f16 v[78:81], v[120:123], v[100:103], v[78:81]
	ds_read_b128 v[136:139], v92
	v_mfma_f32_16x16x32_f16 v[74:77], v[124:127], v[100:103], v[74:77]
	ds_read_b128 v[156:159], v94 offset:2048
	v_mfma_f32_16x16x32_f16 v[70:73], v[128:131], v[100:103], v[70:73]
	ds_read_b128 v[140:143], v92 offset:2048
	v_mfma_f32_16x16x32_f16 v[62:65], v[132:135], v[100:103], v[62:65]
	ds_read_b128 v[160:163], v94 offset:4096
	v_mfma_f32_16x16x32_f16 v[58:61], v[116:119], v[104:107], v[58:61]
	ds_read_b128 v[144:147], v92 offset:4096
	v_mfma_f32_16x16x32_f16 v[54:57], v[120:123], v[104:107], v[54:57]
	ds_read_b128 v[164:167], v94 offset:6144
	v_mfma_f32_16x16x32_f16 v[50:53], v[124:127], v[104:107], v[50:53]
	ds_read_b128 v[148:151], v92 offset:6144
	v_mfma_f32_16x16x32_f16 v[46:49], v[128:131], v[104:107], v[46:49]
	ds_read_b128 v[168:171], v94 offset:8192
	v_mfma_f32_16x16x32_f16 v[42:45], v[132:135], v[104:107], v[42:45]
	v_mfma_f32_16x16x32_f16 v[38:41], v[116:119], v[108:111], v[38:41]
	v_add_u32_e32 v91, s27, v89
	v_mfma_f32_16x16x32_f16 v[30:33], v[120:123], v[108:111], v[30:33]
	v_add_u32_e32 v93, s27, v90
	v_mfma_f32_16x16x32_f16 v[26:29], v[124:127], v[108:111], v[26:29]
	v_xor_b32_e32 v92, 64, v91
	v_mfma_f32_16x16x32_f16 v[22:25], v[128:131], v[108:111], v[22:25]
	v_xor_b32_e32 v94, 64, v93
	v_mfma_f32_16x16x32_f16 v[18:21], v[132:135], v[108:111], v[18:21]
	v_mfma_f32_16x16x32_f16 v[14:17], v[116:119], v[112:115], v[14:17]
	v_mfma_f32_16x16x32_f16 v[10:13], v[120:123], v[112:115], v[10:13]
	v_mfma_f32_16x16x32_f16 v[2:5], v[124:127], v[112:115], v[2:5]
	v_mfma_f32_16x16x32_f16 v[6:9], v[128:131], v[112:115], v[6:9]
	v_mfma_f32_16x16x32_f16 v[66:69], v[132:135], v[112:115], v[66:69]
	s_waitcnt lgkmcnt(0)
	s_barrier
	v_mfma_f32_16x16x32_f16 v[34:37], v[152:155], v[136:139], v[34:37]
	ds_read_b128 v[116:119], v93
	v_mfma_f32_16x16x32_f16 v[78:81], v[156:159], v[136:139], v[78:81]
	ds_read_b128 v[100:103], v91
	v_mfma_f32_16x16x32_f16 v[74:77], v[160:163], v[136:139], v[74:77]
	ds_read_b128 v[120:123], v93 offset:2048
	v_mfma_f32_16x16x32_f16 v[70:73], v[164:167], v[136:139], v[70:73]
	ds_read_b128 v[104:107], v91 offset:2048
	v_mfma_f32_16x16x32_f16 v[62:65], v[168:171], v[136:139], v[62:65]
	ds_read_b128 v[124:127], v93 offset:4096
	v_mfma_f32_16x16x32_f16 v[58:61], v[152:155], v[140:143], v[58:61]
	ds_read_b128 v[108:111], v91 offset:4096
	v_mfma_f32_16x16x32_f16 v[54:57], v[156:159], v[140:143], v[54:57]
	ds_read_b128 v[128:131], v93 offset:6144
	v_mfma_f32_16x16x32_f16 v[50:53], v[160:163], v[140:143], v[50:53]
	ds_read_b128 v[112:115], v91 offset:6144
	v_mfma_f32_16x16x32_f16 v[46:49], v[164:167], v[140:143], v[46:49]
	ds_read_b128 v[132:135], v93 offset:8192
	v_mfma_f32_16x16x32_f16 v[42:45], v[168:171], v[140:143], v[42:45]
	v_mfma_f32_16x16x32_f16 v[38:41], v[152:155], v[144:147], v[38:41]
	v_mfma_f32_16x16x32_f16 v[30:33], v[156:159], v[144:147], v[30:33]
	v_mfma_f32_16x16x32_f16 v[26:29], v[160:163], v[144:147], v[26:29]
	v_mfma_f32_16x16x32_f16 v[22:25], v[164:167], v[144:147], v[22:25]
	v_mfma_f32_16x16x32_f16 v[18:21], v[168:171], v[144:147], v[18:21]
	v_mfma_f32_16x16x32_f16 v[14:17], v[152:155], v[148:151], v[14:17]
	v_mfma_f32_16x16x32_f16 v[10:13], v[156:159], v[148:151], v[10:13]
	v_mfma_f32_16x16x32_f16 v[2:5], v[160:163], v[148:151], v[2:5]
	v_mfma_f32_16x16x32_f16 v[6:9], v[164:167], v[148:151], v[6:9]
	v_mfma_f32_16x16x32_f16 v[66:69], v[168:171], v[148:151], v[66:69]
	s_mov_b32 s17, s27
	s_add_i32 s16, s16, 1
	s_nop 7
